# f32 matrix cores for the prologue absorbed query weight: per-thread f32 VALU dot products replaced by v_mfma_f32_32x32x2_f32 (f32 operands, f32 accumulate), As tile given the 132-float pitch; on top o
# speedup vs baseline: 1.0038x; 1.0019x over previous
.LBB0_70:
	s_ashr_i32 s12, s27, 9
	s_bfe_u32 s10, s27, 0x50004
	s_ashr_i32 s13, s12, 31
	s_waitcnt lgkmcnt(0)
	s_barrier
	s_lshl_b64 s[6:7], s[12:13], 22
	s_add_u32 s6, s2, s6
	s_addc_u32 s7, s3, s7
	s_lshl_b32 s16, s10, 17
	s_add_u32 s16, s6, s16
	s_addc_u32 s17, s7, 0
	v_ashrrev_i32_e32 v14, 5, v1
	v_lshlrev_b32_e32 v4, 2, v24
	v_and_b32_e32 v4, 0x1f0, v4
	v_lshl_add_u32 v10, v14, 9, v4
	v_lshl_add_u32 v11, v14, 14, v4
	v_mul_lo_u32 v8, v14, s23
	v_add_u32_e32 v8, v8, v4
	global_load_dwordx4 v[168:171], v10, s[16:17]
	s_add_u32 s16, s16, 0x2000
	s_addc_u32 s17, s17, 0
	global_load_dwordx4 v[172:175], v10, s[16:17]
	s_add_u32 s16, s16, 0x2000
	s_addc_u32 s17, s17, 0
	global_load_dwordx4 v[176:179], v10, s[16:17]
	s_add_u32 s16, s16, 0x2000
	s_addc_u32 s17, s17, 0
	global_load_dwordx4 v[180:183], v10, s[16:17]
	s_add_u32 s16, s16, 0x2000
	s_addc_u32 s17, s17, 0
	global_load_dwordx4 v[184:187], v10, s[16:17]
	s_add_u32 s16, s16, 0x2000
	s_addc_u32 s17, s17, 0
	global_load_dwordx4 v[188:191], v10, s[16:17]
	s_add_u32 s16, s16, 0x2000
	s_addc_u32 s17, s17, 0
	global_load_dwordx4 v[192:195], v10, s[16:17]
	s_add_u32 s16, s16, 0x2000
	s_addc_u32 s17, s17, 0
	global_load_dwordx4 v[196:199], v10, s[16:17]
	s_add_u32 s16, s16, 0x2000
	s_addc_u32 s17, s17, 0
	global_load_dwordx4 v[200:203], v10, s[16:17]
	s_add_u32 s16, s16, 0x2000
	s_addc_u32 s17, s17, 0
	global_load_dwordx4 v[204:207], v10, s[16:17]
	s_add_u32 s16, s16, 0x2000
	s_addc_u32 s17, s17, 0
	global_load_dwordx4 v[208:211], v10, s[16:17]
	s_add_u32 s16, s16, 0x2000
	s_addc_u32 s17, s17, 0
	global_load_dwordx4 v[212:215], v10, s[16:17]
	s_add_u32 s16, s16, 0x2000
	s_addc_u32 s17, s17, 0
	global_load_dwordx4 v[216:219], v10, s[16:17]
	s_add_u32 s16, s16, 0x2000
	s_addc_u32 s17, s17, 0
	global_load_dwordx4 v[16:19], v10, s[16:17]
	s_add_u32 s16, s16, 0x2000
	s_addc_u32 s17, s17, 0
	global_load_dwordx4 v[20:23], v10, s[16:17]
	s_add_u32 s16, s16, 0x2000
	s_addc_u32 s17, s17, 0
	global_load_dwordx4 v[26:29], v10, s[16:17]
	s_lshl_b32 s6, s27, 5
	s_and_b32 s29, s6, 0x1e0
	s_lshl_b64 s[16:17], s[12:13], 9
	s_or_b32 s16, s16, s29
	s_lshl_b32 s6, s10, 9
	s_add_u32 s18, s0, s6
	s_addc_u32 s19, s1, 0
	s_lshl_b64 s[16:17], s[16:17], 14
	s_add_u32 s16, s18, s16
	s_addc_u32 s17, s19, s17
	global_load_dwordx4 v[30:33], v11, s[16:17]
	s_add_u32 s16, s16, 0x40000
	s_addc_u32 s17, s17, 0
	global_load_dwordx4 v[34:37], v11, s[16:17]
	v_add_u32_e32 v9, s25, v8
	v_add_u32_e32 v12, 0x10800, v8
	s_waitcnt vmcnt(17)
	ds_write_b128 v8, v[168:171]
	s_waitcnt vmcnt(16)
	ds_write_b128 v8, v[172:175] offset:8448
	s_waitcnt vmcnt(15)
	ds_write_b128 v8, v[176:179] offset:16896
	s_waitcnt vmcnt(14)
	ds_write_b128 v8, v[180:183] offset:25344
	s_waitcnt vmcnt(13)
	ds_write_b128 v8, v[184:187] offset:33792
	s_waitcnt vmcnt(12)
	ds_write_b128 v8, v[188:191] offset:42240
	s_waitcnt vmcnt(11)
	ds_write_b128 v8, v[192:195] offset:50688
	s_waitcnt vmcnt(10)
	ds_write_b128 v8, v[196:199] offset:59136
	s_waitcnt vmcnt(9)
	ds_write_b128 v12, v[200:203]
	s_waitcnt vmcnt(8)
	ds_write_b128 v12, v[204:207] offset:8448
	s_waitcnt vmcnt(7)
	ds_write_b128 v12, v[208:211] offset:16896
	s_waitcnt vmcnt(6)
	ds_write_b128 v12, v[212:215] offset:25344
	s_waitcnt vmcnt(5)
	ds_write_b128 v12, v[216:219] offset:33792
	s_waitcnt vmcnt(4)
	ds_write_b128 v12, v[16:19] offset:42240
	s_waitcnt vmcnt(3)
	ds_write_b128 v12, v[20:23] offset:50688
	s_waitcnt vmcnt(2)
	ds_write_b128 v12, v[26:29] offset:59136
	s_waitcnt vmcnt(1)
	ds_write_b128 v9, v[30:33]
	s_waitcnt vmcnt(0)
	ds_write_b128 v9, v[34:37] offset:8448
	s_waitcnt lgkmcnt(0)
	s_barrier
	v_and_b32_e32 v4, 31, v1
	v_bfe_u32 v10, v1, 5, 1
	v_lshrrev_b32_e32 v11, 6, v1
	v_lshl_or_b32 v12, v11, 5, v4
	v_mul_u32_u24_e32 v13, 0x210, v12
	v_lshl_add_u32 v13, v10, 8, v13
	v_mul_u32_u24_e32 v14, 0x210, v4
	v_lshl_add_u32 v14, v10, 8, v14
	v_add_u32_e32 v14, s25, v14
	ds_read_b128 v[80:83], v14
	ds_read_b128 v[144:147], v13
	ds_read_b128 v[84:87], v14 offset:16
	ds_read_b128 v[148:151], v13 offset:16
	ds_read_b128 v[88:91], v14 offset:32
	ds_read_b128 v[152:155], v13 offset:32
	ds_read_b128 v[92:95], v14 offset:48
	ds_read_b128 v[156:159], v13 offset:48
	ds_read_b128 v[96:99], v14 offset:64
	ds_read_b128 v[160:163], v13 offset:64
	ds_read_b128 v[100:103], v14 offset:80
	ds_read_b128 v[164:167], v13 offset:80
	ds_read_b128 v[104:107], v14 offset:96
	ds_read_b128 v[168:171], v13 offset:96
	ds_read_b128 v[108:111], v14 offset:112
	ds_read_b128 v[172:175], v13 offset:112
	ds_read_b128 v[112:115], v14 offset:128
	ds_read_b128 v[176:179], v13 offset:128
	ds_read_b128 v[116:119], v14 offset:144
	ds_read_b128 v[180:183], v13 offset:144
	ds_read_b128 v[120:123], v14 offset:160
	ds_read_b128 v[184:187], v13 offset:160
	ds_read_b128 v[124:127], v14 offset:176
	ds_read_b128 v[188:191], v13 offset:176
	ds_read_b128 v[128:131], v14 offset:192
	ds_read_b128 v[192:195], v13 offset:192
	ds_read_b128 v[132:135], v14 offset:208
	ds_read_b128 v[196:199], v13 offset:208
	ds_read_b128 v[136:139], v14 offset:224
	ds_read_b128 v[200:203], v13 offset:224
	ds_read_b128 v[140:143], v14 offset:240
	ds_read_b128 v[204:207], v13 offset:240
	s_mul_i32 s7, s12, 0x2800
	s_lshl_b32 s6, s10, 8
	s_add_u32 s7, s7, s6
	s_lshl_b32 s7, s7, 10
	s_lshl_b32 s6, s29, 1
	s_add_u32 s7, s7, s6
	s_add_u32 s16, s8, s7
	s_addc_u32 s17, s9, 0
	v_lshlrev_b32_e32 v12, 10, v12
	v_lshl_add_u32 v12, v10, 3, v12
	s_waitcnt lgkmcnt(0)
	v_mfma_f32_32x32x2_f32 v[56:71], v80, v144, 0
	v_mfma_f32_32x32x2_f32 v[56:71], v81, v145, v[56:71]
	v_mfma_f32_32x32x2_f32 v[56:71], v82, v146, v[56:71]
	v_mfma_f32_32x32x2_f32 v[56:71], v83, v147, v[56:71]
	v_mfma_f32_32x32x2_f32 v[56:71], v84, v148, v[56:71]
	v_mfma_f32_32x32x2_f32 v[56:71], v85, v149, v[56:71]
	v_mfma_f32_32x32x2_f32 v[56:71], v86, v150, v[56:71]
	v_mfma_f32_32x32x2_f32 v[56:71], v87, v151, v[56:71]
	v_mfma_f32_32x32x2_f32 v[56:71], v88, v152, v[56:71]
	v_mfma_f32_32x32x2_f32 v[56:71], v89, v153, v[56:71]
	v_mfma_f32_32x32x2_f32 v[56:71], v90, v154, v[56:71]
	v_mfma_f32_32x32x2_f32 v[56:71], v91, v155, v[56:71]
	v_mfma_f32_32x32x2_f32 v[56:71], v92, v156, v[56:71]
	v_mfma_f32_32x32x2_f32 v[56:71], v93, v157, v[56:71]
	v_mfma_f32_32x32x2_f32 v[56:71], v94, v158, v[56:71]
	v_mfma_f32_32x32x2_f32 v[56:71], v95, v159, v[56:71]
	v_mfma_f32_32x32x2_f32 v[56:71], v96, v160, v[56:71]
	v_mfma_f32_32x32x2_f32 v[56:71], v97, v161, v[56:71]
	v_mfma_f32_32x32x2_f32 v[56:71], v98, v162, v[56:71]
	v_mfma_f32_32x32x2_f32 v[56:71], v99, v163, v[56:71]
	v_mfma_f32_32x32x2_f32 v[56:71], v100, v164, v[56:71]
	v_mfma_f32_32x32x2_f32 v[56:71], v101, v165, v[56:71]
	v_mfma_f32_32x32x2_f32 v[56:71], v102, v166, v[56:71]
	v_mfma_f32_32x32x2_f32 v[56:71], v103, v167, v[56:71]
	v_mfma_f32_32x32x2_f32 v[56:71], v104, v168, v[56:71]
	v_mfma_f32_32x32x2_f32 v[56:71], v105, v169, v[56:71]
	v_mfma_f32_32x32x2_f32 v[56:71], v106, v170, v[56:71]
	v_mfma_f32_32x32x2_f32 v[56:71], v107, v171, v[56:71]
	v_mfma_f32_32x32x2_f32 v[56:71], v108, v172, v[56:71]
	v_mfma_f32_32x32x2_f32 v[56:71], v109, v173, v[56:71]
	v_mfma_f32_32x32x2_f32 v[56:71], v110, v174, v[56:71]
	v_mfma_f32_32x32x2_f32 v[56:71], v111, v175, v[56:71]
	v_mfma_f32_32x32x2_f32 v[56:71], v112, v176, v[56:71]
	v_mfma_f32_32x32x2_f32 v[56:71], v113, v177, v[56:71]
	v_mfma_f32_32x32x2_f32 v[56:71], v114, v178, v[56:71]
	v_mfma_f32_32x32x2_f32 v[56:71], v115, v179, v[56:71]
	v_mfma_f32_32x32x2_f32 v[56:71], v116, v180, v[56:71]
	v_mfma_f32_32x32x2_f32 v[56:71], v117, v181, v[56:71]
	v_mfma_f32_32x32x2_f32 v[56:71], v118, v182, v[56:71]
	v_mfma_f32_32x32x2_f32 v[56:71], v119, v183, v[56:71]
	v_mfma_f32_32x32x2_f32 v[56:71], v120, v184, v[56:71]
	v_mfma_f32_32x32x2_f32 v[56:71], v121, v185, v[56:71]
	v_mfma_f32_32x32x2_f32 v[56:71], v122, v186, v[56:71]
	v_mfma_f32_32x32x2_f32 v[56:71], v123, v187, v[56:71]
	v_mfma_f32_32x32x2_f32 v[56:71], v124, v188, v[56:71]
	v_mfma_f32_32x32x2_f32 v[56:71], v125, v189, v[56:71]
	v_mfma_f32_32x32x2_f32 v[56:71], v126, v190, v[56:71]
	v_mfma_f32_32x32x2_f32 v[56:71], v127, v191, v[56:71]
	v_mfma_f32_32x32x2_f32 v[56:71], v128, v192, v[56:71]
	v_mfma_f32_32x32x2_f32 v[56:71], v129, v193, v[56:71]
	v_mfma_f32_32x32x2_f32 v[56:71], v130, v194, v[56:71]
	v_mfma_f32_32x32x2_f32 v[56:71], v131, v195, v[56:71]
	v_mfma_f32_32x32x2_f32 v[56:71], v132, v196, v[56:71]
	v_mfma_f32_32x32x2_f32 v[56:71], v133, v197, v[56:71]
	v_mfma_f32_32x32x2_f32 v[56:71], v134, v198, v[56:71]
	v_mfma_f32_32x32x2_f32 v[56:71], v135, v199, v[56:71]
	v_mfma_f32_32x32x2_f32 v[56:71], v136, v200, v[56:71]
	v_mfma_f32_32x32x2_f32 v[56:71], v137, v201, v[56:71]
	v_mfma_f32_32x32x2_f32 v[56:71], v138, v202, v[56:71]
	v_mfma_f32_32x32x2_f32 v[56:71], v139, v203, v[56:71]
	v_mfma_f32_32x32x2_f32 v[56:71], v140, v204, v[56:71]
	v_mfma_f32_32x32x2_f32 v[56:71], v141, v205, v[56:71]
	v_mfma_f32_32x32x2_f32 v[56:71], v142, v206, v[56:71]
	v_mfma_f32_32x32x2_f32 v[56:71], v143, v207, v[56:71]
	s_add_i32 s27, s27, s28
	s_nop 15
	s_nop 3
	v_cvt_pk_bf16_f32 v40, v56, v57
	v_cvt_pk_bf16_f32 v41, v58, v59
	v_cvt_pk_bf16_f32 v42, v60, v61
	v_cvt_pk_bf16_f32 v43, v62, v63
	v_cvt_pk_bf16_f32 v44, v64, v65
	v_cvt_pk_bf16_f32 v45, v66, v67
	v_cvt_pk_bf16_f32 v46, v68, v69
	v_cvt_pk_bf16_f32 v47, v70, v71
	global_store_dwordx2 v12, v[40:41], s[16:17]
	global_store_dwordx2 v12, v[42:43], s[16:17] offset:16
	global_store_dwordx2 v12, v[44:45], s[16:17] offset:32
	global_store_dwordx2 v12, v[46:47], s[16:17] offset:48
	s_cmpk_gt_i32 s27, 0x3ff
	s_cbranch_scc0 .LBB0_70
